# v23 with one unexecuted 4-byte pad before the P2 loop head: every hot loop head back at the baseline's mod-8 byte phase (code placement test)
# speedup vs baseline: 1.0010x; 1.0010x over previous
.LBB0_344:
	s_waitcnt lgkmcnt(0)
	s_add_i32 s4, s60, 0x180
	s_add_i32 s5, s36, 0x180
	s_barrier
	s_setprio 1
	s_waitcnt lgkmcnt(7)
	v_mfma_f32_16x16x32_bf16 v[60:63], v[164:167], v[196:199], 0
	s_waitcnt lgkmcnt(6)
	v_mfma_f32_16x16x32_bf16 v[60:63], v[160:163], v[192:195], v[60:63]
	v_mfma_f32_16x16x32_bf16 v[56:59], v[156:159], v[196:199], 0
	s_nop 0
	v_mfma_f32_16x16x32_bf16 v[56:59], v[152:155], v[192:195], v[56:59]
	s_waitcnt lgkmcnt(5)
	v_mfma_f32_16x16x32_bf16 v[52:55], v[164:167], v[188:191], 0
	s_waitcnt lgkmcnt(4)
	v_mfma_f32_16x16x32_bf16 v[52:55], v[160:163], v[184:187], v[52:55]
	v_mfma_f32_16x16x32_bf16 v[48:51], v[156:159], v[188:191], 0
	s_nop 0
	v_mfma_f32_16x16x32_bf16 v[48:51], v[152:155], v[184:187], v[48:51]
	s_waitcnt lgkmcnt(3)
	v_mfma_f32_16x16x32_bf16 v[44:47], v[164:167], v[180:183], 0
	s_waitcnt lgkmcnt(2)
	v_mfma_f32_16x16x32_bf16 v[44:47], v[160:163], v[176:179], v[44:47]
	v_mfma_f32_16x16x32_bf16 v[40:43], v[156:159], v[180:183], 0
	s_nop 0
	v_mfma_f32_16x16x32_bf16 v[40:43], v[152:155], v[176:179], v[40:43]
	s_waitcnt lgkmcnt(1)
	v_mfma_f32_16x16x32_bf16 v[36:39], v[164:167], v[172:175], 0
	s_waitcnt lgkmcnt(0)
	v_mfma_f32_16x16x32_bf16 v[36:39], v[160:163], v[168:171], v[36:39]
	v_mfma_f32_16x16x32_bf16 v[32:35], v[156:159], v[172:175], 0
	s_nop 0
	v_mfma_f32_16x16x32_bf16 v[32:35], v[152:155], v[168:171], v[32:35]
	s_setprio 0
	s_setprio 1
	v_mfma_f32_16x16x32_bf16 v[28:31], v[148:151], v[196:199], 0
	s_nop 0
	v_mfma_f32_16x16x32_bf16 v[28:31], v[144:147], v[192:195], v[28:31]
	v_mfma_f32_16x16x32_bf16 v[24:27], v[140:143], v[196:199], 0
	s_nop 0
	v_mfma_f32_16x16x32_bf16 v[24:27], v[136:139], v[192:195], v[24:27]
	v_mfma_f32_16x16x32_bf16 v[20:23], v[148:151], v[188:191], 0
	s_nop 0
	v_mfma_f32_16x16x32_bf16 v[20:23], v[144:147], v[184:187], v[20:23]
	v_mfma_f32_16x16x32_bf16 v[16:19], v[140:143], v[188:191], 0
	s_nop 0
	v_mfma_f32_16x16x32_bf16 v[16:19], v[136:139], v[184:187], v[16:19]
	v_mfma_f32_16x16x32_bf16 v[12:15], v[148:151], v[180:183], 0
	s_nop 0
	v_mfma_f32_16x16x32_bf16 v[12:15], v[144:147], v[176:179], v[12:15]
	v_mfma_f32_16x16x32_bf16 v[8:11], v[140:143], v[180:183], 0
	s_nop 0
	v_mfma_f32_16x16x32_bf16 v[8:11], v[136:139], v[176:179], v[8:11]
	v_mfma_f32_16x16x32_bf16 v[4:7], v[148:151], v[172:175], 0
	s_nop 0
	v_mfma_f32_16x16x32_bf16 v[4:7], v[144:147], v[168:171], v[4:7]
	v_mfma_f32_16x16x32_bf16 v[0:3], v[140:143], v[172:175], 0
	s_nop 0
	v_mfma_f32_16x16x32_bf16 v[0:3], v[136:139], v[168:171], v[0:3]
	s_setprio 0
	s_barrier
	ds_read_b128 v[164:167], v225
	ds_read_b128 v[160:163], v226
	ds_read_b128 v[156:159], v227
	ds_read_b128 v[152:155], v228
	ds_read_b128 v[148:151], v229
	ds_read_b128 v[144:147], v230
	ds_read_b128 v[140:143], v231
	ds_read_b128 v[136:139], v232
	ds_read_b128 v[168:171], v233 offset:32768
	ds_read_b128 v[172:175], v233 offset:33792
	ds_read_b128 v[176:179], v233 offset:34816
	ds_read_b128 v[180:183], v233 offset:35840
	ds_read_b128 v[184:187], v233 offset:36864
	ds_read_b128 v[188:191], v233 offset:37888
	ds_read_b128 v[192:195], v233 offset:38912
	ds_read_b128 v[196:199], v233 offset:39936
	s_mov_b32 m0, s72
	s_add_i32 s14, s60, 0x100100
	buffer_load_dwordx4 v214, s[8:11], s14 offen lds
	s_add_i32 s14, s60, 0x180100
	s_mov_b32 m0, s73
	s_nop 0
	buffer_load_dwordx4 v214, s[8:11], s14 offen lds
	s_waitcnt vmcnt(10)
	s_waitcnt lgkmcnt(8)
	s_barrier
	s_setprio 1
	s_waitcnt lgkmcnt(7)
	v_mfma_f32_16x16x32_bf16 v[124:127], v[164:167], v[168:171], v[124:127]
	s_waitcnt lgkmcnt(6)
	v_mfma_f32_16x16x32_bf16 v[124:127], v[160:163], v[172:175], v[124:127]
	v_mfma_f32_16x16x32_bf16 v[120:123], v[156:159], v[168:171], v[120:123]
	s_nop 0
	v_mfma_f32_16x16x32_bf16 v[120:123], v[152:155], v[172:175], v[120:123]
	s_waitcnt lgkmcnt(5)
	v_mfma_f32_16x16x32_bf16 v[116:119], v[164:167], v[176:179], v[116:119]
	s_waitcnt lgkmcnt(4)
	v_mfma_f32_16x16x32_bf16 v[116:119], v[160:163], v[180:183], v[116:119]
	v_mfma_f32_16x16x32_bf16 v[112:115], v[156:159], v[176:179], v[112:115]
	s_nop 0
	v_mfma_f32_16x16x32_bf16 v[112:115], v[152:155], v[180:183], v[112:115]
	s_waitcnt lgkmcnt(3)
	v_mfma_f32_16x16x32_bf16 v[108:111], v[164:167], v[184:187], v[108:111]
	s_waitcnt lgkmcnt(2)
	v_mfma_f32_16x16x32_bf16 v[108:111], v[160:163], v[188:191], v[108:111]
	v_mfma_f32_16x16x32_bf16 v[104:107], v[156:159], v[184:187], v[104:107]
	s_nop 0
	v_mfma_f32_16x16x32_bf16 v[104:107], v[152:155], v[188:191], v[104:107]
	s_waitcnt lgkmcnt(1)
	v_mfma_f32_16x16x32_bf16 v[100:103], v[164:167], v[192:195], v[100:103]
	s_waitcnt lgkmcnt(0)
	v_mfma_f32_16x16x32_bf16 v[100:103], v[160:163], v[196:199], v[100:103]
	v_mfma_f32_16x16x32_bf16 v[96:99], v[156:159], v[192:195], v[96:99]
	s_nop 0
	v_mfma_f32_16x16x32_bf16 v[96:99], v[152:155], v[196:199], v[96:99]
	s_setprio 0
	s_setprio 1
	v_mfma_f32_16x16x32_bf16 v[92:95], v[148:151], v[168:171], v[92:95]
	s_nop 0
	v_mfma_f32_16x16x32_bf16 v[92:95], v[144:147], v[172:175], v[92:95]
	v_mfma_f32_16x16x32_bf16 v[88:91], v[140:143], v[168:171], v[88:91]
	s_nop 0
	v_mfma_f32_16x16x32_bf16 v[88:91], v[136:139], v[172:175], v[88:91]
	v_mfma_f32_16x16x32_bf16 v[84:87], v[148:151], v[176:179], v[84:87]
	s_nop 0
	v_mfma_f32_16x16x32_bf16 v[84:87], v[144:147], v[180:183], v[84:87]
	v_mfma_f32_16x16x32_bf16 v[80:83], v[140:143], v[176:179], v[80:83]
	s_nop 0
	v_mfma_f32_16x16x32_bf16 v[80:83], v[136:139], v[180:183], v[80:83]
	v_mfma_f32_16x16x32_bf16 v[76:79], v[148:151], v[184:187], v[76:79]
	s_nop 0
	v_mfma_f32_16x16x32_bf16 v[76:79], v[144:147], v[188:191], v[76:79]
	v_mfma_f32_16x16x32_bf16 v[72:75], v[140:143], v[184:187], v[72:75]
	s_nop 0
	v_mfma_f32_16x16x32_bf16 v[72:75], v[136:139], v[188:191], v[72:75]
	v_mfma_f32_16x16x32_bf16 v[68:71], v[148:151], v[192:195], v[68:71]
	s_nop 0
	v_mfma_f32_16x16x32_bf16 v[68:71], v[144:147], v[196:199], v[68:71]
	v_mfma_f32_16x16x32_bf16 v[64:67], v[140:143], v[192:195], v[64:67]
	s_nop 0
	v_mfma_f32_16x16x32_bf16 v[64:67], v[136:139], v[196:199], v[64:67]
	s_setprio 0
	s_barrier
	ds_read_b128 v[168:171], v233 offset:49152
	ds_read_b128 v[172:175], v233 offset:50176
	ds_read_b128 v[176:179], v233 offset:51200
	ds_read_b128 v[180:183], v233 offset:52224
	ds_read_b128 v[184:187], v233 offset:53248
	ds_read_b128 v[188:191], v233 offset:54272
	ds_read_b128 v[192:195], v233 offset:55296
	ds_read_b128 v[196:199], v233 offset:56320
	s_mov_b32 m0, s76
	s_mov_b32 s14, s10
	s_mov_b32 s15, s11
	buffer_load_dwordx4 v215, s[12:15], s5 offen lds
	s_add_i32 s5, s36, 0x100180
	s_mov_b32 m0, s77
	s_nop 0
	buffer_load_dwordx4 v215, s[12:15], s5 offen lds
	s_add_i32 s5, s36, 0x10180
	s_mov_b32 m0, s80
	s_nop 0
	buffer_load_dwordx4 v215, s[12:15], s5 offen lds
	s_add_i32 s5, s36, 0x110180
	s_mov_b32 m0, s81
	s_nop 0
	buffer_load_dwordx4 v215, s[12:15], s5 offen lds
	s_mov_b32 m0, s78
	s_nop 0
	buffer_load_dwordx4 v214, s[8:11], s4 offen lds
	s_add_i32 s4, s60, 0x80180
	s_mov_b32 m0, s79
	s_nop 0
	buffer_load_dwordx4 v214, s[8:11], s4 offen lds
	s_waitcnt vmcnt(8)
	s_waitcnt lgkmcnt(6)
	s_barrier
	s_setprio 1
	s_waitcnt lgkmcnt(7)
	v_mfma_f32_16x16x32_bf16 v[60:63], v[164:167], v[168:171], v[60:63]
	s_waitcnt lgkmcnt(6)
	v_mfma_f32_16x16x32_bf16 v[60:63], v[160:163], v[172:175], v[60:63]
	v_mfma_f32_16x16x32_bf16 v[56:59], v[156:159], v[168:171], v[56:59]
	s_nop 0
	v_mfma_f32_16x16x32_bf16 v[56:59], v[152:155], v[172:175], v[56:59]
	s_waitcnt lgkmcnt(5)
	v_mfma_f32_16x16x32_bf16 v[52:55], v[164:167], v[176:179], v[52:55]
	s_waitcnt lgkmcnt(4)
	v_mfma_f32_16x16x32_bf16 v[52:55], v[160:163], v[180:183], v[52:55]
	v_mfma_f32_16x16x32_bf16 v[48:51], v[156:159], v[176:179], v[48:51]
	s_nop 0
	v_mfma_f32_16x16x32_bf16 v[48:51], v[152:155], v[180:183], v[48:51]
	s_waitcnt lgkmcnt(3)
	v_mfma_f32_16x16x32_bf16 v[44:47], v[164:167], v[184:187], v[44:47]
	s_waitcnt lgkmcnt(2)
	v_mfma_f32_16x16x32_bf16 v[44:47], v[160:163], v[188:191], v[44:47]
	v_mfma_f32_16x16x32_bf16 v[40:43], v[156:159], v[184:187], v[40:43]
	s_nop 0
	v_mfma_f32_16x16x32_bf16 v[40:43], v[152:155], v[188:191], v[40:43]
	s_waitcnt lgkmcnt(1)
	v_mfma_f32_16x16x32_bf16 v[36:39], v[164:167], v[192:195], v[36:39]
	s_waitcnt lgkmcnt(0)
	v_mfma_f32_16x16x32_bf16 v[36:39], v[160:163], v[196:199], v[36:39]
	v_mfma_f32_16x16x32_bf16 v[32:35], v[156:159], v[192:195], v[32:35]
	s_nop 0
	v_mfma_f32_16x16x32_bf16 v[32:35], v[152:155], v[196:199], v[32:35]
	s_setprio 0
	s_setprio 1
	v_mfma_f32_16x16x32_bf16 v[28:31], v[148:151], v[168:171], v[28:31]
	s_nop 0
	v_mfma_f32_16x16x32_bf16 v[28:31], v[144:147], v[172:175], v[28:31]
	v_mfma_f32_16x16x32_bf16 v[24:27], v[140:143], v[168:171], v[24:27]
	s_nop 0
	v_mfma_f32_16x16x32_bf16 v[24:27], v[136:139], v[172:175], v[24:27]
	v_mfma_f32_16x16x32_bf16 v[20:23], v[148:151], v[176:179], v[20:23]
	s_nop 0
	v_mfma_f32_16x16x32_bf16 v[20:23], v[144:147], v[180:183], v[20:23]
	v_mfma_f32_16x16x32_bf16 v[16:19], v[140:143], v[176:179], v[16:19]
	s_nop 0
	v_mfma_f32_16x16x32_bf16 v[16:19], v[136:139], v[180:183], v[16:19]
	v_mfma_f32_16x16x32_bf16 v[12:15], v[148:151], v[184:187], v[12:15]
	s_nop 0
	v_mfma_f32_16x16x32_bf16 v[12:15], v[144:147], v[188:191], v[12:15]
	v_mfma_f32_16x16x32_bf16 v[8:11], v[140:143], v[184:187], v[8:11]
	s_nop 0
	v_mfma_f32_16x16x32_bf16 v[8:11], v[136:139], v[188:191], v[8:11]
	v_mfma_f32_16x16x32_bf16 v[4:7], v[148:151], v[192:195], v[4:7]
	s_nop 0
	v_mfma_f32_16x16x32_bf16 v[4:7], v[144:147], v[196:199], v[4:7]
	v_mfma_f32_16x16x32_bf16 v[0:3], v[140:143], v[192:195], v[0:3]
	s_nop 0
	v_mfma_f32_16x16x32_bf16 v[0:3], v[136:139], v[196:199], v[0:3]
	s_setprio 0
	s_barrier
	s_waitcnt vmcnt(14)
	v_mul_f32_e32 v132, 0x42800000, v132
	v_mul_f32_e32 v128, 0x42800000, v128
	v_mul_f32_e32 v133, 0x42800000, v133
	v_mul_f32_e32 v129, 0x42800000, v129
	v_mul_f32_e32 v134, 0x42800000, v134
	v_mul_f32_e32 v130, 0x42800000, v130
	v_mul_f32_e32 v135, 0x42800000, v135
	v_mul_f32_e32 v131, 0x42800000, v131
	v_cvt_pk_fp8_f32 v204, v128, v132
	v_cvt_pk_fp8_f32 v234, v129, v133
	v_cvt_pk_fp8_f32 v235, v130, v134
	v_cvt_pk_fp8_f32 v236, v131, v135
	s_add_i32 s33, s36, 0x200
	s_mov_b32 s61, 0
	s_mov_b32 s66, s75
	s_mov_b32 s94, s86
	s_branch .LBB0_347
	s_nop 0
